# all 640 unit-scale f8 MFMAs in the plain v_mfma_f32_16x16x128_f8f6f4 form, on top of the one-operand-per-step MFMA order
# speedup vs baseline: 1.0045x; 1.0045x over previous
.LBB0_332:
	s_add_u32 s6, s61, s4
	s_addc_u32 s7, s62, s5
	s_add_u32 s6, s6, 0x32800100
	s_addc_u32 s7, s7, 0
	s_add_u32 s24, s63, s4
	s_addc_u32 s25, s68, s5
	s_add_i32 s64, 0, 0x10000
	s_cmpk_eq_i32 s4, 0x2a00
	s_cselect_b32 s13, s1, s7
	s_cselect_b32 s12, s0, s6
	s_cselect_b32 s7, s29, s25
	s_cselect_b32 s6, s28, s24
	s_add_i32 s65, 0, 0x14000
	v_add_u32_e32 v2, s64, v188
	v_add_u32_e32 v6, s65, v188
	ds_read_b128 v[26:29], v2
	ds_read_b128 v[30:33], v2 offset:1024
	ds_read_b128 v[18:21], v2 offset:2048
	ds_read_b128 v[22:25], v2 offset:3072
	ds_read_b128 v[10:13], v6
	ds_read_b128 v[14:17], v6 offset:1024
	ds_read_b128 v[2:5], v6 offset:2048
	ds_read_b128 v[6:9], v6 offset:3072
	v_lshl_add_u64 v[214:215], v[168:169], 0, s[4:5]
	s_add_i32 m0, s18, 0xc000
	ds_read_b128 v[172:175], v189
	ds_read_b128 v[176:179], v189 offset:1024
	ds_read_b128 v[190:193], v189 offset:2048
	ds_read_b128 v[194:197], v189 offset:3072
	ds_read_b128 v[198:201], v189 offset:4096
	ds_read_b128 v[202:205], v189 offset:5120
	ds_read_b128 v[206:209], v189 offset:6144
	ds_read_b128 v[210:213], v189 offset:7168
	global_load_lds_dwordx4 v[214:215], off
	v_lshl_add_u64 v[214:215], v[170:171], 0, s[4:5]
	s_add_i32 m0, s18, 0xe000
	s_nop 0
	global_load_lds_dwordx4 v[214:215], off
	s_waitcnt vmcnt(8)
	s_waitcnt lgkmcnt(0)
	s_barrier
	s_setprio 1
	s_waitcnt lgkmcnt(0)
	v_mfma_f32_16x16x128_f8f6f4 v[70:73], v[26:33], v[172:179], v[70:73]
	v_mfma_f32_16x16x128_f8f6f4 v[66:69], v[18:25], v[172:179], v[66:69]
	v_mfma_f32_16x16x128_f8f6f4 v[74:77], v[18:25], v[190:197], v[74:77]
	v_mfma_f32_16x16x128_f8f6f4 v[78:81], v[26:33], v[190:197], v[78:81]
	v_mfma_f32_16x16x128_f8f6f4 v[86:89], v[26:33], v[198:205], v[86:89]
	v_mfma_f32_16x16x128_f8f6f4 v[82:85], v[18:25], v[198:205], v[82:85]
	v_mfma_f32_16x16x128_f8f6f4 v[90:93], v[18:25], v[206:213], v[90:93]
	v_mfma_f32_16x16x128_f8f6f4 v[94:97], v[26:33], v[206:213], v[94:97]
	s_setprio 0
	s_setprio 1
	v_mfma_f32_16x16x128_f8f6f4 v[134:137], v[10:17], v[206:213], v[134:137]
	v_mfma_f32_16x16x128_f8f6f4 v[130:133], v[2:9], v[206:213], v[130:133]
	v_mfma_f32_16x16x128_f8f6f4 v[154:157], v[2:9], v[172:179], v[154:157]
	v_mfma_f32_16x16x128_f8f6f4 v[158:161], v[10:17], v[172:179], v[158:161]
	v_mfma_f32_16x16x128_f8f6f4 v[150:153], v[10:17], v[190:197], v[150:153]
	v_mfma_f32_16x16x128_f8f6f4 v[146:149], v[2:9], v[190:197], v[146:149]
	v_mfma_f32_16x16x128_f8f6f4 v[138:141], v[2:9], v[198:205], v[138:141]
	v_mfma_f32_16x16x128_f8f6f4 v[142:145], v[10:17], v[198:205], v[142:145]
	s_setprio 0
	s_barrier
	s_add_i32 s24, s64, s17
	v_lshl_add_u64 v[172:173], s[6:7], 0, v[162:163]
	s_mov_b32 m0, s24
	ds_read_b128 v[190:193], v189 offset:16384
	ds_read_b128 v[194:197], v189 offset:17408
	ds_read_b128 v[198:201], v189 offset:18432
	ds_read_b128 v[202:205], v189 offset:19456
	ds_read_b128 v[206:209], v189 offset:20480
	ds_read_b128 v[210:213], v189 offset:21504
	ds_read_b128 v[214:217], v189 offset:22528
	ds_read_b128 v[218:221], v189 offset:23552
	global_load_lds_dwordx4 v[172:173], off
	s_add_i32 m0, s24, 0x2000
	s_add_u32 s24, s6, 0x158000
	v_lshl_add_u64 v[174:175], s[6:7], 0, v[166:167]
	s_addc_u32 s25, s7, 0
	s_add_i32 s64, s65, s17
	global_load_lds_dwordx4 v[174:175], off
	v_lshl_add_u64 v[176:177], s[24:25], 0, v[162:163]
	s_mov_b32 m0, s64
	v_lshl_add_u64 v[178:179], s[12:13], 0, v[166:167]
	global_load_lds_dwordx4 v[176:177], off
	v_lshl_add_u64 v[176:177], s[24:25], 0, v[166:167]
	s_add_i32 m0, s64, 0x2000
	s_nop 0
	global_load_lds_dwordx4 v[176:177], off
	v_lshl_add_u64 v[176:177], s[12:13], 0, v[162:163]
	s_mov_b32 m0, s18
	s_nop 0
	global_load_lds_dwordx4 v[176:177], off
	s_mov_b32 m0, s19
	s_nop 0
	global_load_lds_dwordx4 v[178:179], off
	s_waitcnt vmcnt(8)
	s_waitcnt lgkmcnt(0)
	s_barrier
	s_setprio 1
	s_waitcnt lgkmcnt(0)
	v_mfma_f32_16x16x128_f8f6f4 v[110:113], v[26:33], v[198:205], v[110:113]
	v_mfma_f32_16x16x128_f8f6f4 v[106:109], v[18:25], v[198:205], v[106:109]
	v_mfma_f32_16x16x128_f8f6f4 v[98:101], v[18:25], v[190:197], v[98:101]
	v_mfma_f32_16x16x128_f8f6f4 v[102:105], v[26:33], v[190:197], v[102:105]
	v_mfma_f32_16x16x128_f8f6f4 v[118:121], v[26:33], v[206:213], v[118:121]
	v_mfma_f32_16x16x128_f8f6f4 v[114:117], v[18:25], v[206:213], v[114:117]
	v_mfma_f32_16x16x128_f8f6f4 v[122:125], v[18:25], v[214:221], v[122:125]
	v_mfma_f32_16x16x128_f8f6f4 v[126:129], v[26:33], v[214:221], v[126:129]
	s_setprio 0
	s_setprio 1
	v_mfma_f32_16x16x128_f8f6f4 v[62:65], v[10:17], v[214:221], v[62:65]
	v_mfma_f32_16x16x128_f8f6f4 v[58:61], v[2:9], v[214:221], v[58:61]
	v_mfma_f32_16x16x128_f8f6f4 v[34:37], v[2:9], v[190:197], v[34:37]
	v_mfma_f32_16x16x128_f8f6f4 v[38:41], v[10:17], v[190:197], v[38:41]
	v_mfma_f32_16x16x128_f8f6f4 v[46:49], v[10:17], v[198:205], v[46:49]
	v_mfma_f32_16x16x128_f8f6f4 v[42:45], v[2:9], v[198:205], v[42:45]
	v_mfma_f32_16x16x128_f8f6f4 v[50:53], v[2:9], v[206:213], v[50:53]
	v_mfma_f32_16x16x128_f8f6f4 v[54:57], v[10:17], v[206:213], v[54:57]
	s_setprio 0
	s_barrier
	s_add_i32 s24, 0, 0x18000
	s_add_i32 s25, 0, 0x1c000
	v_add_u32_e32 v14, s24, v188
	v_add_u32_e32 v30, s25, v188
	ds_read_b128 v[2:5], v14
	ds_read_b128 v[6:9], v14 offset:1024
	ds_read_b128 v[10:13], v14 offset:2048
	ds_read_b128 v[14:17], v14 offset:3072
	ds_read_b128 v[18:21], v30
	ds_read_b128 v[22:25], v30 offset:1024
	ds_read_b128 v[26:29], v30 offset:2048
	ds_read_b128 v[30:33], v30 offset:3072
	s_add_u32 s12, s12, 0x158000
	s_addc_u32 s13, s13, 0
	s_mov_b32 m0, s93
	v_lshl_add_u64 v[222:223], s[12:13], 0, v[162:163]
	ds_read_b128 v[190:193], v189 offset:32768
	ds_read_b128 v[194:197], v189 offset:33792
	ds_read_b128 v[198:201], v189 offset:34816
	ds_read_b128 v[202:205], v189 offset:35840
	ds_read_b128 v[206:209], v189 offset:36864
	ds_read_b128 v[210:213], v189 offset:37888
	ds_read_b128 v[214:217], v189 offset:38912
	ds_read_b128 v[218:221], v189 offset:39936
	global_load_lds_dwordx4 v[222:223], off
	v_lshl_add_u64 v[222:223], s[12:13], 0, v[166:167]
	s_mov_b32 m0, s94
	s_nop 0
	global_load_lds_dwordx4 v[222:223], off
	s_waitcnt vmcnt(8)
	s_waitcnt lgkmcnt(0)
	s_barrier
	s_setprio 1
	s_waitcnt lgkmcnt(0)
	v_mfma_f32_16x16x128_f8f6f4 v[82:85], v[10:17], v[206:213], v[82:85]
	v_mfma_f32_16x16x128_f8f6f4 v[86:89], v[2:9], v[206:213], v[86:89]
	v_mfma_f32_16x16x128_f8f6f4 v[70:73], v[2:9], v[190:197], v[70:73]
	v_mfma_f32_16x16x128_f8f6f4 v[66:69], v[10:17], v[190:197], v[66:69]
	v_mfma_f32_16x16x128_f8f6f4 v[74:77], v[10:17], v[198:205], v[74:77]
	v_mfma_f32_16x16x128_f8f6f4 v[78:81], v[2:9], v[198:205], v[78:81]
	v_mfma_f32_16x16x128_f8f6f4 v[94:97], v[2:9], v[214:221], v[94:97]
	v_mfma_f32_16x16x128_f8f6f4 v[90:93], v[10:17], v[214:221], v[90:93]
	s_setprio 0
	s_setprio 1
	v_mfma_f32_16x16x128_f8f6f4 v[134:137], v[18:25], v[214:221], v[134:137]
	v_mfma_f32_16x16x128_f8f6f4 v[130:133], v[26:33], v[214:221], v[130:133]
	v_mfma_f32_16x16x128_f8f6f4 v[154:157], v[26:33], v[190:197], v[154:157]
	v_mfma_f32_16x16x128_f8f6f4 v[158:161], v[18:25], v[190:197], v[158:161]
	v_mfma_f32_16x16x128_f8f6f4 v[150:153], v[18:25], v[198:205], v[150:153]
	v_mfma_f32_16x16x128_f8f6f4 v[146:149], v[26:33], v[198:205], v[146:149]
	v_mfma_f32_16x16x128_f8f6f4 v[138:141], v[26:33], v[206:213], v[138:141]
	v_mfma_f32_16x16x128_f8f6f4 v[142:145], v[18:25], v[206:213], v[142:145]
	s_setprio 0
	s_barrier
	s_add_i32 s12, s24, s17
	v_lshl_add_u64 v[172:173], v[172:173], 0, s[76:77]
	s_mov_b32 m0, s12
	ds_read_b128 v[190:193], v189 offset:49152
	ds_read_b128 v[194:197], v189 offset:50176
	ds_read_b128 v[198:201], v189 offset:51200
	ds_read_b128 v[202:205], v189 offset:52224
	ds_read_b128 v[206:209], v189 offset:53248
	ds_read_b128 v[210:213], v189 offset:54272
	ds_read_b128 v[214:217], v189 offset:55296
	ds_read_b128 v[218:221], v189 offset:56320
	global_load_lds_dwordx4 v[172:173], off
	s_add_i32 m0, s12, 0x2000
	s_add_u32 s6, s6, 0x158080
	v_lshl_add_u64 v[172:173], v[174:175], 0, s[76:77]
	s_addc_u32 s7, s7, 0
	s_add_i32 s12, s25, s17
	global_load_lds_dwordx4 v[172:173], off
	v_lshl_add_u64 v[172:173], s[6:7], 0, v[162:163]
	s_mov_b32 m0, s12
	s_nop 0
	global_load_lds_dwordx4 v[172:173], off
	v_lshl_add_u64 v[172:173], s[6:7], 0, v[166:167]
	s_add_i32 m0, s12, 0x2000
	s_nop 0
	global_load_lds_dwordx4 v[172:173], off
	v_lshl_add_u64 v[172:173], v[176:177], 0, s[76:77]
	s_mov_b32 m0, s95
	s_nop 0
	global_load_lds_dwordx4 v[172:173], off
	v_lshl_add_u64 v[172:173], v[178:179], 0, s[76:77]
	s_mov_b32 m0, vcc_lo
	s_nop 0
	global_load_lds_dwordx4 v[172:173], off
	s_waitcnt vmcnt(8)
	s_waitcnt lgkmcnt(0)
	s_barrier
	s_setprio 1
	s_waitcnt lgkmcnt(0)
	v_mfma_f32_16x16x128_f8f6f4 v[118:121], v[2:9], v[206:213], v[118:121]
	v_mfma_f32_16x16x128_f8f6f4 v[114:117], v[10:17], v[206:213], v[114:117]
	v_mfma_f32_16x16x128_f8f6f4 v[98:101], v[10:17], v[190:197], v[98:101]
	v_mfma_f32_16x16x128_f8f6f4 v[102:105], v[2:9], v[190:197], v[102:105]
	v_mfma_f32_16x16x128_f8f6f4 v[110:113], v[2:9], v[198:205], v[110:113]
	v_mfma_f32_16x16x128_f8f6f4 v[106:109], v[10:17], v[198:205], v[106:109]
	v_mfma_f32_16x16x128_f8f6f4 v[122:125], v[10:17], v[214:221], v[122:125]
	v_mfma_f32_16x16x128_f8f6f4 v[126:129], v[2:9], v[214:221], v[126:129]
	s_setprio 0
	s_setprio 1
	v_mfma_f32_16x16x128_f8f6f4 v[62:65], v[18:25], v[214:221], v[62:65]
	v_mfma_f32_16x16x128_f8f6f4 v[58:61], v[26:33], v[214:221], v[58:61]
	v_mfma_f32_16x16x128_f8f6f4 v[34:37], v[26:33], v[190:197], v[34:37]
	v_mfma_f32_16x16x128_f8f6f4 v[38:41], v[18:25], v[190:197], v[38:41]
	v_mfma_f32_16x16x128_f8f6f4 v[46:49], v[18:25], v[198:205], v[46:49]
	v_mfma_f32_16x16x128_f8f6f4 v[42:45], v[26:33], v[198:205], v[42:45]
	v_mfma_f32_16x16x128_f8f6f4 v[50:53], v[26:33], v[206:213], v[50:53]
	v_mfma_f32_16x16x128_f8f6f4 v[54:57], v[18:25], v[206:213], v[54:57]
	s_setprio 0
	s_barrier
	s_add_i32 vcc_hi, vcc_hi, 2
	s_add_u32 s4, s4, 0x100
	s_addc_u32 s5, s5, 0
	s_cmpk_lt_u32 vcc_hi, 0x54
	s_cbranch_scc1 .LBB0_332
	s_waitcnt vmcnt(0)
	s_mov_b64 s[12:13], s[54:55]
	s_cmpk_gt_u32 s89, 0xff
	s_cbranch_scc1 .LBB0_335
	s_barrier

.LBB0_1437:
	v_and_b32_e32 v188, 15, v189
	v_and_b32_e32 v2, 48, v189
	v_lshlrev_b32_e32 v3, 2, v189
	s_and_b32 s8, s6, 3
	s_lshl_b32 s9, s7, 13
	v_lshl_or_b32 v2, v188, 6, v2
	v_and_b32_e32 v3, 32, v3
	v_bitop3_b32 v4, v2, s9, v3 bitop3:0xde
	s_lshl_b32 s9, s8, 12
	v_lshl_add_u64 v[180:181], s[20:21], 0, v[154:155]
	v_bitop3_b32 v2, v2, s9, v3 bitop3:0xde
	s_add_i32 s9, s60, s72
	v_lshl_add_u64 v[178:179], s[20:21], 0, v[182:183]
	v_lshl_add_u64 v[72:73], v[180:181], 0, s[36:37]
	s_mov_b32 m0, s9
	s_add_i32 s19, s9, 0x2000
	s_waitcnt vmcnt(2)
	s_barrier
	global_load_lds_dwordx4 v[72:73], off
	v_lshl_add_u64 v[158:159], v[178:179], 0, s[36:37]
	s_mov_b32 m0, s19
	s_add_i32 s18, s67, 0x8000
	global_load_lds_dwordx4 v[158:159], off
	v_lshl_add_u64 v[70:71], v[172:173], 0, s[36:37]
	s_mov_b32 m0, s18
	s_add_i32 s43, s67, 0xa000
	global_load_lds_dwordx4 v[70:71], off
	v_lshl_add_u64 v[160:161], v[170:171], 0, s[36:37]
	s_mov_b32 m0, s43
	s_add_i32 s44, s61, s72
	global_load_lds_dwordx4 v[160:161], off
	v_lshl_add_u64 v[162:163], s[24:25], 0, v[154:155]
	s_mov_b32 m0, s44
	s_add_i32 s45, s44, 0x2000
	global_load_lds_dwordx4 v[162:163], off
	v_lshl_add_u64 v[164:165], s[24:25], 0, v[182:183]
	s_mov_b32 m0, s45
	s_add_i32 s73, 0, 0x10000
	global_load_lds_dwordx4 v[164:165], off
	v_add_u32_e32 v195, s73, v2
	s_add_i32 s75, 0, 0x14000
	s_waitcnt vmcnt(6)
	s_barrier
	v_add_u32_e32 v194, s75, v2
	v_add_u32_e32 v191, 0, v4
	v_add_u32_e32 v193, s60, v2
	v_add_u32_e32 v192, s61, v2
	ds_read_b128 v[54:57], v195
	ds_read_b128 v[58:61], v195 offset:1024
	ds_read_b128 v[196:199], v195 offset:2048
	ds_read_b128 v[200:203], v195 offset:3072
	ds_read_b128 v[10:13], v194
	ds_read_b128 v[14:17], v194 offset:1024
	ds_read_b128 v[2:5], v194 offset:2048
	ds_read_b128 v[6:9], v194 offset:3072
	s_lshl_b32 s66, s7, 6
	v_lshl_add_u64 v[176:177], s[22:23], 0, v[154:155]
	v_lshl_add_u64 v[174:175], s[22:23], 0, v[182:183]
	s_add_u32 s70, s4, 0x10080
	s_addc_u32 s71, s5, 0
	s_add_i32 s74, s67, 0xc000
	v_lshl_add_u64 v[30:31], s[70:71], 0, v[154:155]
	s_mov_b32 m0, s74
	s_add_i32 s69, s67, 0xe000
	ds_read_b128 v[22:25], v191
	ds_read_b128 v[26:29], v191 offset:1024
	ds_read_b128 v[34:37], v191 offset:2048
	ds_read_b128 v[38:41], v191 offset:3072
	ds_read_b128 v[82:85], v191 offset:4096
	ds_read_b128 v[86:89], v191 offset:5120
	ds_read_b128 v[94:97], v191 offset:6144
	ds_read_b128 v[98:101], v191 offset:7168
	global_load_lds_dwordx4 v[30:31], off
	v_lshl_add_u64 v[30:31], s[70:71], 0, v[182:183]
	s_mov_b32 m0, s69
	s_nop 0
	global_load_lds_dwordx4 v[30:31], off
	s_waitcnt vmcnt(8)
	s_waitcnt lgkmcnt(0)
	s_barrier
	s_setprio 1
	v_mov_b64_e32 v[32:33], v[20:21]
	v_mov_b64_e32 v[152:153], v[20:21]
	v_mov_b64_e32 v[92:93], v[20:21]
	v_mov_b64_e32 v[44:45], v[20:21]
	v_mov_b64_e32 v[116:117], v[20:21]
	v_mov_b64_e32 v[64:65], v[20:21]
	v_mov_b64_e32 v[80:81], v[20:21]
	v_mov_b64_e32 v[52:53], v[20:21]
	v_mov_b64_e32 v[30:31], v[18:19]
	v_mov_b64_e32 v[150:151], v[18:19]
	v_mov_b64_e32 v[90:91], v[18:19]
	v_mov_b64_e32 v[42:43], v[18:19]
	v_mov_b64_e32 v[114:115], v[18:19]
	v_mov_b64_e32 v[62:63], v[18:19]
	v_mov_b64_e32 v[78:79], v[18:19]
	v_mov_b64_e32 v[50:51], v[18:19]
	s_waitcnt lgkmcnt(0)
	v_mfma_f32_16x16x128_f8f6f4 v[30:33], v[54:61], v[22:29], v[30:33]
	v_mfma_f32_16x16x128_f8f6f4 v[150:153], v[196:203], v[22:29], v[150:153]
	v_mfma_f32_16x16x128_f8f6f4 v[42:45], v[196:203], v[34:41], v[42:45]
	v_mfma_f32_16x16x128_f8f6f4 v[90:93], v[54:61], v[34:41], v[90:93]
	v_mfma_f32_16x16x128_f8f6f4 v[114:117], v[54:61], v[82:89], v[114:117]
	v_mfma_f32_16x16x128_f8f6f4 v[62:65], v[196:203], v[82:89], v[62:65]
	v_mfma_f32_16x16x128_f8f6f4 v[50:53], v[196:203], v[94:101], v[50:53]
	v_mfma_f32_16x16x128_f8f6f4 v[78:81], v[54:61], v[94:101], v[78:81]
	s_setprio 0
	s_setprio 1
	v_mov_b64_e32 v[144:145], v[20:21]
	v_mov_b64_e32 v[148:149], v[20:21]
	v_mov_b64_e32 v[142:143], v[18:19]
	v_mov_b64_e32 v[146:147], v[18:19]
	v_mfma_f32_16x16x128_f8f6f4 v[142:145], v[10:17], v[22:29], v[142:145]
	v_mfma_f32_16x16x128_f8f6f4 v[146:149], v[2:9], v[22:29], v[146:149]
	v_mov_b64_e32 v[28:29], v[20:21]
	v_mov_b64_e32 v[140:141], v[20:21]
	v_mov_b64_e32 v[26:27], v[18:19]
	v_mov_b64_e32 v[138:139], v[18:19]
	v_mfma_f32_16x16x128_f8f6f4 v[26:29], v[10:17], v[34:41], v[26:29]
	v_mfma_f32_16x16x128_f8f6f4 v[138:141], v[2:9], v[34:41], v[138:141]
	v_mov_b64_e32 v[40:41], v[20:21]
	v_mov_b64_e32 v[128:129], v[20:21]
	v_mov_b64_e32 v[24:25], v[20:21]
	v_mov_b64_e32 v[76:77], v[20:21]
	v_mov_b64_e32 v[38:39], v[18:19]
	v_mov_b64_e32 v[126:127], v[18:19]
	v_mov_b64_e32 v[22:23], v[18:19]
	v_mov_b64_e32 v[74:75], v[18:19]
	v_mfma_f32_16x16x128_f8f6f4 v[38:41], v[10:17], v[82:89], v[38:41]
	v_mfma_f32_16x16x128_f8f6f4 v[126:129], v[2:9], v[82:89], v[126:129]
	v_mfma_f32_16x16x128_f8f6f4 v[22:25], v[10:17], v[94:101], v[22:25]
	v_mfma_f32_16x16x128_f8f6f4 v[74:77], v[2:9], v[94:101], v[74:77]
	s_setprio 0
	s_barrier
	s_add_i32 s70, s73, s72
	v_lshl_add_u64 v[34:35], v[180:181], 0, s[14:15]
	s_mov_b32 m0, s70
	s_add_i32 s71, s70, 0x2000
	ds_read_b128 v[204:207], v191 offset:16384
	ds_read_b128 v[208:211], v191 offset:17408
	ds_read_b128 v[212:215], v191 offset:18432
	ds_read_b128 v[216:219], v191 offset:19456
	ds_read_b128 v[220:223], v191 offset:20480
	ds_read_b128 v[224:227], v191 offset:21504
	ds_read_b128 v[228:231], v191 offset:22528
	ds_read_b128 v[232:235], v191 offset:23552
	global_load_lds_dwordx4 v[34:35], off
	v_lshl_add_u64 v[34:35], v[178:179], 0, s[14:15]
	s_mov_b32 m0, s71
	s_add_i32 s72, s75, s72
	global_load_lds_dwordx4 v[34:35], off
	v_lshl_add_u64 v[34:35], s[26:27], 0, v[154:155]
	s_mov_b32 m0, s72
	s_add_i32 s73, s72, 0x2000
	global_load_lds_dwordx4 v[34:35], off
	v_lshl_add_u64 v[34:35], s[26:27], 0, v[182:183]
	s_mov_b32 m0, s73
	s_nop 0
	global_load_lds_dwordx4 v[34:35], off
	v_lshl_add_u64 v[34:35], v[172:173], 0, s[14:15]
	s_mov_b32 m0, s67
	s_nop 0
	global_load_lds_dwordx4 v[34:35], off
	v_lshl_add_u64 v[34:35], v[170:171], 0, s[14:15]
	s_mov_b32 m0, s68
	s_nop 0
	global_load_lds_dwordx4 v[34:35], off
	s_waitcnt vmcnt(8)
	s_waitcnt lgkmcnt(0)
	s_barrier
	s_setprio 1
	v_mov_b64_e32 v[136:137], v[20:21]
	v_mov_b64_e32 v[104:105], v[20:21]
	v_mov_b64_e32 v[124:125], v[20:21]
	v_mov_b64_e32 v[100:101], v[20:21]
	v_mov_b64_e32 v[112:113], v[20:21]
	v_mov_b64_e32 v[108:109], v[20:21]
	v_mov_b64_e32 v[88:89], v[20:21]
	v_mov_b64_e32 v[84:85], v[20:21]
	v_mov_b64_e32 v[134:135], v[18:19]
	v_mov_b64_e32 v[102:103], v[18:19]
	v_mov_b64_e32 v[122:123], v[18:19]
	v_mov_b64_e32 v[98:99], v[18:19]
	v_mov_b64_e32 v[110:111], v[18:19]
	v_mov_b64_e32 v[106:107], v[18:19]
	v_mov_b64_e32 v[86:87], v[18:19]
	v_mov_b64_e32 v[82:83], v[18:19]
	s_waitcnt lgkmcnt(0)
	v_mfma_f32_16x16x128_f8f6f4 v[134:137], v[54:61], v[204:211], v[134:137]
	v_mfma_f32_16x16x128_f8f6f4 v[102:105], v[196:203], v[204:211], v[102:105]
	v_mfma_f32_16x16x128_f8f6f4 v[98:101], v[196:203], v[212:219], v[98:101]
	v_mfma_f32_16x16x128_f8f6f4 v[122:125], v[54:61], v[212:219], v[122:125]
	v_mfma_f32_16x16x128_f8f6f4 v[110:113], v[54:61], v[220:227], v[110:113]
	v_mfma_f32_16x16x128_f8f6f4 v[106:109], v[196:203], v[220:227], v[106:109]
	v_mfma_f32_16x16x128_f8f6f4 v[82:85], v[196:203], v[228:235], v[82:85]
	v_mfma_f32_16x16x128_f8f6f4 v[86:89], v[54:61], v[228:235], v[86:89]
	s_setprio 0
	s_setprio 1
	v_mov_b64_e32 v[36:37], v[20:21]
	v_mov_b64_e32 v[132:133], v[20:21]
	v_mov_b64_e32 v[48:49], v[20:21]
	v_mov_b64_e32 v[120:121], v[20:21]
	v_mov_b64_e32 v[68:69], v[20:21]
	v_mov_b64_e32 v[96:97], v[20:21]
	v_mov_b64_e32 v[56:57], v[20:21]
	v_mov_b64_e32 v[60:61], v[20:21]
	v_mov_b64_e32 v[34:35], v[18:19]
	v_mov_b64_e32 v[130:131], v[18:19]
	v_mov_b64_e32 v[46:47], v[18:19]
	v_mov_b64_e32 v[118:119], v[18:19]
	v_mov_b64_e32 v[66:67], v[18:19]
	v_mov_b64_e32 v[94:95], v[18:19]
	v_mov_b64_e32 v[54:55], v[18:19]
	v_mov_b64_e32 v[58:59], v[18:19]
	v_mfma_f32_16x16x128_f8f6f4 v[54:57], v[10:17], v[228:235], v[54:57]
	v_mfma_f32_16x16x128_f8f6f4 v[58:61], v[2:9], v[228:235], v[58:61]
	v_mfma_f32_16x16x128_f8f6f4 v[130:133], v[2:9], v[204:211], v[130:133]
	v_mfma_f32_16x16x128_f8f6f4 v[34:37], v[10:17], v[204:211], v[34:37]
	v_mfma_f32_16x16x128_f8f6f4 v[46:49], v[10:17], v[212:219], v[46:49]
	v_mfma_f32_16x16x128_f8f6f4 v[118:121], v[2:9], v[212:219], v[118:121]
	v_mfma_f32_16x16x128_f8f6f4 v[94:97], v[2:9], v[220:227], v[94:97]
	v_mfma_f32_16x16x128_f8f6f4 v[66:69], v[10:17], v[220:227], v[66:69]
	s_setprio 0
	s_barrier
	ds_read_b128 v[2:5], v193
	ds_read_b128 v[6:9], v193 offset:1024
	ds_read_b128 v[10:13], v193 offset:2048
	ds_read_b128 v[14:17], v193 offset:3072
	ds_read_b128 v[196:199], v192
	ds_read_b128 v[200:203], v192 offset:1024
	ds_read_b128 v[204:207], v192 offset:2048
	ds_read_b128 v[208:211], v192 offset:3072
	s_add_u32 s76, s4, 0x10100
	s_addc_u32 s77, s5, 0
	s_mov_b32 m0, s48
	v_lshl_add_u64 v[244:245], s[76:77], 0, v[154:155]
	ds_read_b128 v[212:215], v191 offset:32768
	ds_read_b128 v[216:219], v191 offset:33792
	ds_read_b128 v[220:223], v191 offset:34816
	ds_read_b128 v[224:227], v191 offset:35840
	ds_read_b128 v[228:231], v191 offset:36864
	ds_read_b128 v[232:235], v191 offset:37888
	ds_read_b128 v[236:239], v191 offset:38912
	ds_read_b128 v[240:243], v191 offset:39936
	global_load_lds_dwordx4 v[244:245], off
	v_lshl_add_u64 v[244:245], s[76:77], 0, v[182:183]
	s_mov_b32 m0, s49
	s_nop 0
	global_load_lds_dwordx4 v[244:245], off
	s_waitcnt vmcnt(8)
	s_waitcnt lgkmcnt(0)
	s_barrier
	s_setprio 1
	s_waitcnt lgkmcnt(0)
	v_mfma_f32_16x16x128_f8f6f4 v[42:45], v[10:17], v[220:227], v[42:45]
	v_mfma_f32_16x16x128_f8f6f4 v[90:93], v[2:9], v[220:227], v[90:93]
	v_mfma_f32_16x16x128_f8f6f4 v[30:33], v[2:9], v[212:219], v[30:33]
	v_mfma_f32_16x16x128_f8f6f4 v[150:153], v[10:17], v[212:219], v[150:153]
	v_mfma_f32_16x16x128_f8f6f4 v[62:65], v[10:17], v[228:235], v[62:65]
	v_mfma_f32_16x16x128_f8f6f4 v[114:117], v[2:9], v[228:235], v[114:117]
	v_mfma_f32_16x16x128_f8f6f4 v[78:81], v[2:9], v[236:243], v[78:81]
	v_mfma_f32_16x16x128_f8f6f4 v[50:53], v[10:17], v[236:243], v[50:53]
	s_setprio 0
	s_setprio 1
	v_mfma_f32_16x16x128_f8f6f4 v[22:25], v[196:203], v[236:243], v[22:25]
	v_mfma_f32_16x16x128_f8f6f4 v[74:77], v[204:211], v[236:243], v[74:77]
	v_mfma_f32_16x16x128_f8f6f4 v[146:149], v[204:211], v[212:219], v[146:149]
	v_mfma_f32_16x16x128_f8f6f4 v[142:145], v[196:203], v[212:219], v[142:145]
	v_mfma_f32_16x16x128_f8f6f4 v[26:29], v[196:203], v[220:227], v[26:29]
	v_mfma_f32_16x16x128_f8f6f4 v[138:141], v[204:211], v[220:227], v[138:141]
	v_mfma_f32_16x16x128_f8f6f4 v[126:129], v[204:211], v[228:235], v[126:129]
	v_mfma_f32_16x16x128_f8f6f4 v[38:41], v[196:203], v[228:235], v[38:41]
	s_setprio 0
	s_barrier
	s_mov_b32 m0, s9
	v_lshl_add_u64 v[244:245], v[180:181], 0, s[38:39]
	ds_read_b128 v[212:215], v191 offset:49152
	ds_read_b128 v[216:219], v191 offset:50176
	ds_read_b128 v[220:223], v191 offset:51200
	ds_read_b128 v[224:227], v191 offset:52224
	ds_read_b128 v[228:231], v191 offset:53248
	ds_read_b128 v[232:235], v191 offset:54272
	ds_read_b128 v[236:239], v191 offset:55296
	ds_read_b128 v[240:243], v191 offset:56320
	global_load_lds_dwordx4 v[244:245], off
	v_lshl_add_u64 v[244:245], v[178:179], 0, s[38:39]
	s_mov_b32 m0, s19
	s_nop 0
	global_load_lds_dwordx4 v[244:245], off
	v_lshl_add_u64 v[244:245], s[28:29], 0, v[154:155]
	s_mov_b32 m0, s44
	s_nop 0
	global_load_lds_dwordx4 v[244:245], off
	v_lshl_add_u64 v[244:245], s[28:29], 0, v[182:183]
	s_mov_b32 m0, s45
	s_nop 0
	global_load_lds_dwordx4 v[244:245], off
	v_lshl_add_u64 v[244:245], v[172:173], 0, s[38:39]
	s_mov_b32 m0, s18
	s_nop 0
	global_load_lds_dwordx4 v[244:245], off
	v_lshl_add_u64 v[244:245], v[170:171], 0, s[38:39]
	s_mov_b32 m0, s43
	s_nop 0
	global_load_lds_dwordx4 v[244:245], off
	s_waitcnt vmcnt(8)
	s_waitcnt lgkmcnt(0)
	s_barrier
	s_setprio 1
	s_waitcnt lgkmcnt(0)
	v_mfma_f32_16x16x128_f8f6f4 v[110:113], v[2:9], v[228:235], v[110:113]
	v_mfma_f32_16x16x128_f8f6f4 v[106:109], v[10:17], v[228:235], v[106:109]
	v_mfma_f32_16x16x128_f8f6f4 v[102:105], v[10:17], v[212:219], v[102:105]
	v_mfma_f32_16x16x128_f8f6f4 v[134:137], v[2:9], v[212:219], v[134:137]
	v_mfma_f32_16x16x128_f8f6f4 v[122:125], v[2:9], v[220:227], v[122:125]
	v_mfma_f32_16x16x128_f8f6f4 v[98:101], v[10:17], v[220:227], v[98:101]
	v_mfma_f32_16x16x128_f8f6f4 v[82:85], v[10:17], v[236:243], v[82:85]
	v_mfma_f32_16x16x128_f8f6f4 v[86:89], v[2:9], v[236:243], v[86:89]
	s_setprio 0
	s_setprio 1
	v_mfma_f32_16x16x128_f8f6f4 v[54:57], v[196:203], v[236:243], v[54:57]
	v_mfma_f32_16x16x128_f8f6f4 v[58:61], v[204:211], v[236:243], v[58:61]
	v_mfma_f32_16x16x128_f8f6f4 v[130:133], v[204:211], v[212:219], v[130:133]
	v_mfma_f32_16x16x128_f8f6f4 v[34:37], v[196:203], v[212:219], v[34:37]
	v_mfma_f32_16x16x128_f8f6f4 v[46:49], v[196:203], v[220:227], v[46:49]
	v_mfma_f32_16x16x128_f8f6f4 v[118:121], v[204:211], v[220:227], v[118:121]
	v_mfma_f32_16x16x128_f8f6f4 v[94:97], v[204:211], v[228:235], v[94:97]
	v_mfma_f32_16x16x128_f8f6f4 v[66:69], v[196:203], v[228:235], v[66:69]
	s_setprio 0
	s_barrier
	ds_read_b128 v[2:5], v195
	ds_read_b128 v[6:9], v195 offset:1024
	ds_read_b128 v[10:13], v195 offset:2048
	ds_read_b128 v[14:17], v195 offset:3072
	ds_read_b128 v[196:199], v194
	ds_read_b128 v[200:203], v194 offset:1024
	ds_read_b128 v[204:207], v194 offset:2048
	ds_read_b128 v[208:211], v194 offset:3072
	s_add_u32 s4, s4, 0x10180
	s_addc_u32 s5, s5, 0
	s_mov_b32 m0, s74
	v_lshl_add_u64 v[194:195], s[4:5], 0, v[154:155]
	ds_read_b128 v[212:215], v191
	ds_read_b128 v[216:219], v191 offset:1024
	ds_read_b128 v[220:223], v191 offset:2048
	ds_read_b128 v[224:227], v191 offset:3072
	ds_read_b128 v[228:231], v191 offset:4096
	ds_read_b128 v[232:235], v191 offset:5120
	ds_read_b128 v[236:239], v191 offset:6144
	ds_read_b128 v[240:243], v191 offset:7168
	global_load_lds_dwordx4 v[194:195], off
	v_lshl_add_u64 v[182:183], s[4:5], 0, v[182:183]
	s_mov_b32 m0, s69
	s_nop 0
	global_load_lds_dwordx4 v[182:183], off
	s_waitcnt vmcnt(8)
	s_waitcnt lgkmcnt(0)
	s_barrier
	s_setprio 1
	s_waitcnt lgkmcnt(0)
	v_mfma_f32_16x16x128_f8f6f4 v[114:117], v[2:9], v[228:235], v[114:117]
	v_mfma_f32_16x16x128_f8f6f4 v[62:65], v[10:17], v[228:235], v[62:65]
	v_mfma_f32_16x16x128_f8f6f4 v[150:153], v[10:17], v[212:219], v[150:153]
	v_mfma_f32_16x16x128_f8f6f4 v[30:33], v[2:9], v[212:219], v[30:33]
	v_mfma_f32_16x16x128_f8f6f4 v[90:93], v[2:9], v[220:227], v[90:93]
	v_mfma_f32_16x16x128_f8f6f4 v[42:45], v[10:17], v[220:227], v[42:45]
	v_mfma_f32_16x16x128_f8f6f4 v[50:53], v[10:17], v[236:243], v[50:53]
	v_mfma_f32_16x16x128_f8f6f4 v[78:81], v[2:9], v[236:243], v[78:81]
	s_setprio 0
	s_setprio 1
	v_mfma_f32_16x16x128_f8f6f4 v[22:25], v[196:203], v[236:243], v[22:25]
	v_mfma_f32_16x16x128_f8f6f4 v[74:77], v[204:211], v[236:243], v[74:77]
	v_mfma_f32_16x16x128_f8f6f4 v[146:149], v[204:211], v[212:219], v[146:149]
	v_mfma_f32_16x16x128_f8f6f4 v[142:145], v[196:203], v[212:219], v[142:145]
	v_mfma_f32_16x16x128_f8f6f4 v[26:29], v[196:203], v[220:227], v[26:29]
	v_mfma_f32_16x16x128_f8f6f4 v[138:141], v[204:211], v[220:227], v[138:141]
	v_mfma_f32_16x16x128_f8f6f4 v[126:129], v[204:211], v[228:235], v[126:129]
	v_mfma_f32_16x16x128_f8f6f4 v[38:41], v[196:203], v[228:235], v[38:41]
	s_setprio 0
	s_barrier
	s_mov_b32 m0, s70
	ds_read_b128 v[212:215], v191 offset:16384
	ds_read_b128 v[216:219], v191 offset:17408
	ds_read_b128 v[220:223], v191 offset:18432
	ds_read_b128 v[224:227], v191 offset:19456
	ds_read_b128 v[228:231], v191 offset:20480
	ds_read_b128 v[232:235], v191 offset:21504
	ds_read_b128 v[236:239], v191 offset:22528
	ds_read_b128 v[240:243], v191 offset:23552
	global_load_lds_dwordx4 v[180:181], off
	s_mov_b32 m0, s71
	s_nop 0
	global_load_lds_dwordx4 v[178:179], off
	s_mov_b32 m0, s72
	s_nop 0
	global_load_lds_dwordx4 v[176:177], off
	s_mov_b32 m0, s73
	s_nop 0
	global_load_lds_dwordx4 v[174:175], off
	s_mov_b32 m0, s67
	s_nop 0
	global_load_lds_dwordx4 v[172:173], off
	s_mov_b32 m0, s68
	s_nop 0
	global_load_lds_dwordx4 v[170:171], off
	s_waitcnt vmcnt(8)
	s_waitcnt lgkmcnt(0)
	s_barrier
	s_setprio 1
	s_waitcnt lgkmcnt(0)
	v_mfma_f32_16x16x128_f8f6f4 v[110:113], v[2:9], v[228:235], v[110:113]
	v_mfma_f32_16x16x128_f8f6f4 v[106:109], v[10:17], v[228:235], v[106:109]
	v_mfma_f32_16x16x128_f8f6f4 v[102:105], v[10:17], v[212:219], v[102:105]
	v_mfma_f32_16x16x128_f8f6f4 v[134:137], v[2:9], v[212:219], v[134:137]
	v_mfma_f32_16x16x128_f8f6f4 v[122:125], v[2:9], v[220:227], v[122:125]
	v_mfma_f32_16x16x128_f8f6f4 v[98:101], v[10:17], v[220:227], v[98:101]
	v_mfma_f32_16x16x128_f8f6f4 v[82:85], v[10:17], v[236:243], v[82:85]
	v_mfma_f32_16x16x128_f8f6f4 v[86:89], v[2:9], v[236:243], v[86:89]
	s_setprio 0
	s_setprio 1
	v_mfma_f32_16x16x128_f8f6f4 v[54:57], v[196:203], v[236:243], v[54:57]
	v_mfma_f32_16x16x128_f8f6f4 v[58:61], v[204:211], v[236:243], v[58:61]
	v_mfma_f32_16x16x128_f8f6f4 v[130:133], v[204:211], v[212:219], v[130:133]
	v_mfma_f32_16x16x128_f8f6f4 v[34:37], v[196:203], v[212:219], v[34:37]
	v_mfma_f32_16x16x128_f8f6f4 v[46:49], v[196:203], v[220:227], v[46:49]
	v_mfma_f32_16x16x128_f8f6f4 v[118:121], v[204:211], v[220:227], v[118:121]
	v_mfma_f32_16x16x128_f8f6f4 v[94:97], v[204:211], v[228:235], v[94:97]
	v_mfma_f32_16x16x128_f8f6f4 v[66:69], v[196:203], v[228:235], v[66:69]
	s_setprio 0
	s_barrier
	ds_read_b128 v[2:5], v193
	ds_read_b128 v[6:9], v193 offset:1024
	ds_read_b128 v[10:13], v193 offset:2048
	ds_read_b128 v[14:17], v193 offset:3072
	ds_read_b128 v[170:173], v192
	ds_read_b128 v[174:177], v192 offset:1024
	ds_read_b128 v[194:197], v192 offset:2048
	ds_read_b128 v[198:201], v192 offset:3072
	s_mov_b32 m0, s48
	ds_read_b128 v[202:205], v191 offset:32768
	ds_read_b128 v[206:209], v191 offset:33792
	ds_read_b128 v[210:213], v191 offset:34816
	ds_read_b128 v[214:217], v191 offset:35840
	ds_read_b128 v[218:221], v191 offset:36864
	ds_read_b128 v[222:225], v191 offset:37888
	ds_read_b128 v[226:229], v191 offset:38912
	ds_read_b128 v[230:233], v191 offset:39936
	global_load_lds_dwordx4 v[166:167], off
	s_mov_b32 m0, s49
	s_nop 0
	global_load_lds_dwordx4 v[168:169], off
	s_waitcnt vmcnt(8)
	s_waitcnt lgkmcnt(0)
	s_barrier
	s_setprio 1
	s_waitcnt lgkmcnt(0)
	v_mfma_f32_16x16x128_f8f6f4 v[30:33], v[2:9], v[202:209], v[30:33]
	v_mfma_f32_16x16x128_f8f6f4 v[150:153], v[10:17], v[202:209], v[150:153]
	v_mfma_f32_16x16x128_f8f6f4 v[42:45], v[10:17], v[210:217], v[42:45]
	v_mfma_f32_16x16x128_f8f6f4 v[90:93], v[2:9], v[210:217], v[90:93]
	v_mfma_f32_16x16x128_f8f6f4 v[114:117], v[2:9], v[218:225], v[114:117]
	v_mfma_f32_16x16x128_f8f6f4 v[62:65], v[10:17], v[218:225], v[62:65]
	v_mfma_f32_16x16x128_f8f6f4 v[50:53], v[10:17], v[226:233], v[50:53]
	v_mfma_f32_16x16x128_f8f6f4 v[78:81], v[2:9], v[226:233], v[78:81]
	s_setprio 0
	s_setprio 1
	v_mfma_f32_16x16x128_f8f6f4 v[22:25], v[170:177], v[226:233], v[22:25]
	v_mfma_f32_16x16x128_f8f6f4 v[74:77], v[194:201], v[226:233], v[74:77]
	v_mfma_f32_16x16x128_f8f6f4 v[146:149], v[194:201], v[202:209], v[146:149]
	v_mfma_f32_16x16x128_f8f6f4 v[142:145], v[170:177], v[202:209], v[142:145]
	v_mfma_f32_16x16x128_f8f6f4 v[26:29], v[170:177], v[210:217], v[26:29]
	v_mfma_f32_16x16x128_f8f6f4 v[138:141], v[194:201], v[210:217], v[138:141]
	v_mfma_f32_16x16x128_f8f6f4 v[126:129], v[194:201], v[218:225], v[126:129]
	v_mfma_f32_16x16x128_f8f6f4 v[38:41], v[170:177], v[218:225], v[38:41]
	s_setprio 0
	s_barrier
	s_mov_b32 m0, s9
	ds_read_b128 v[202:205], v191 offset:49152
	ds_read_b128 v[206:209], v191 offset:50176
	ds_read_b128 v[210:213], v191 offset:51200
	ds_read_b128 v[214:217], v191 offset:52224
	ds_read_b128 v[218:221], v191 offset:53248
	ds_read_b128 v[222:225], v191 offset:54272
	ds_read_b128 v[226:229], v191 offset:55296
	ds_read_b128 v[230:233], v191 offset:56320
	global_load_lds_dwordx4 v[72:73], off
	s_mov_b32 m0, s19
	s_nop 0
	global_load_lds_dwordx4 v[158:159], off
	s_mov_b32 m0, s44
	s_nop 0
	global_load_lds_dwordx4 v[162:163], off
	s_mov_b32 m0, s45
	s_nop 0
	global_load_lds_dwordx4 v[164:165], off
	s_mov_b32 m0, s18
	s_nop 0
	global_load_lds_dwordx4 v[70:71], off
	s_mov_b32 m0, s43
	s_nop 0
	global_load_lds_dwordx4 v[160:161], off
	s_waitcnt vmcnt(8)
	s_waitcnt lgkmcnt(0)
	s_barrier
	s_setprio 1
	s_waitcnt lgkmcnt(0)
	v_mfma_f32_16x16x128_f8f6f4 v[110:113], v[2:9], v[218:225], v[110:113]
	v_mfma_f32_16x16x128_f8f6f4 v[106:109], v[10:17], v[218:225], v[106:109]
	v_mfma_f32_16x16x128_f8f6f4 v[102:105], v[10:17], v[202:209], v[102:105]
	v_mfma_f32_16x16x128_f8f6f4 v[134:137], v[2:9], v[202:209], v[134:137]
	v_mfma_f32_16x16x128_f8f6f4 v[122:125], v[2:9], v[210:217], v[122:125]
	v_mfma_f32_16x16x128_f8f6f4 v[98:101], v[10:17], v[210:217], v[98:101]
	v_mfma_f32_16x16x128_f8f6f4 v[82:85], v[10:17], v[226:233], v[82:85]
	v_mfma_f32_16x16x128_f8f6f4 v[86:89], v[2:9], v[226:233], v[86:89]
	s_setprio 0
	s_setprio 1
	v_mfma_f32_16x16x128_f8f6f4 v[54:57], v[170:177], v[226:233], v[54:57]
	v_mfma_f32_16x16x128_f8f6f4 v[58:61], v[194:201], v[226:233], v[58:61]
	v_mfma_f32_16x16x128_f8f6f4 v[130:133], v[194:201], v[202:209], v[130:133]
	v_mfma_f32_16x16x128_f8f6f4 v[34:37], v[170:177], v[202:209], v[34:37]
	v_mfma_f32_16x16x128_f8f6f4 v[46:49], v[170:177], v[210:217], v[46:49]
	v_mfma_f32_16x16x128_f8f6f4 v[118:121], v[194:201], v[210:217], v[118:121]
	v_mfma_f32_16x16x128_f8f6f4 v[94:97], v[194:201], v[218:225], v[94:97]
	v_mfma_f32_16x16x128_f8f6f4 v[66:69], v[170:177], v[218:225], v[66:69]
	s_setprio 0
	s_barrier
	s_waitcnt vmcnt(0)
	s_cmpk_gt_u32 s65, 0xff
	s_cbranch_scc1 .LBB0_1439
	s_barrier

.LBB0_1745:
	s_add_u32 s8, s49, s6
	s_addc_u32 s9, s50, s7
	s_add_u32 s8, s8, 0x32800100
	s_addc_u32 s9, s9, 0
	s_add_u32 s73, s51, s6
	s_addc_u32 s74, s54, s7
	s_add_i32 s72, 0, 0x10000
	s_cmpk_eq_i32 s6, 0x2a00
	s_cselect_b32 s37, s5, s9
	s_cselect_b32 s36, s4, s8
	s_cselect_b32 s9, s13, s74
	s_cselect_b32 s8, s12, s73
	s_add_i32 s73, 0, 0x14000
	v_add_u32_e32 v2, s72, v188
	v_add_u32_e32 v6, s73, v188
	ds_read_b128 v[26:29], v2
	ds_read_b128 v[30:33], v2 offset:1024
	ds_read_b128 v[18:21], v2 offset:2048
	ds_read_b128 v[22:25], v2 offset:3072
	ds_read_b128 v[10:13], v6
	ds_read_b128 v[14:17], v6 offset:1024
	ds_read_b128 v[2:5], v6 offset:2048
	ds_read_b128 v[6:9], v6 offset:3072
	v_lshl_add_u64 v[214:215], v[168:169], 0, s[6:7]
	s_add_i32 m0, s64, 0xc000
	ds_read_b128 v[172:175], v189
	ds_read_b128 v[176:179], v189 offset:1024
	ds_read_b128 v[190:193], v189 offset:2048
	ds_read_b128 v[194:197], v189 offset:3072
	ds_read_b128 v[198:201], v189 offset:4096
	ds_read_b128 v[202:205], v189 offset:5120
	ds_read_b128 v[206:209], v189 offset:6144
	ds_read_b128 v[210:213], v189 offset:7168
	global_load_lds_dwordx4 v[214:215], off
	v_lshl_add_u64 v[214:215], v[170:171], 0, s[6:7]
	s_add_i32 m0, s64, 0xe000
	s_nop 0
	global_load_lds_dwordx4 v[214:215], off
	s_waitcnt vmcnt(8)
	s_waitcnt lgkmcnt(0)
	s_barrier
	s_setprio 1
	s_waitcnt lgkmcnt(0)
	v_mfma_f32_16x16x128_f8f6f4 v[158:161], v[26:33], v[172:179], v[158:161]
	v_mfma_f32_16x16x128_f8f6f4 v[154:157], v[18:25], v[172:179], v[154:157]
	v_mfma_f32_16x16x128_f8f6f4 v[118:121], v[18:25], v[190:197], v[118:121]
	v_mfma_f32_16x16x128_f8f6f4 v[122:125], v[26:33], v[190:197], v[122:125]
	v_mfma_f32_16x16x128_f8f6f4 v[126:129], v[26:33], v[198:205], v[126:129]
	v_mfma_f32_16x16x128_f8f6f4 v[114:117], v[18:25], v[198:205], v[114:117]
	v_mfma_f32_16x16x128_f8f6f4 v[106:109], v[18:25], v[206:213], v[106:109]
	v_mfma_f32_16x16x128_f8f6f4 v[110:113], v[26:33], v[206:213], v[110:113]
	s_setprio 0
	s_setprio 1
	v_mfma_f32_16x16x128_f8f6f4 v[102:105], v[10:17], v[206:213], v[102:105]
	v_mfma_f32_16x16x128_f8f6f4 v[98:101], v[2:9], v[206:213], v[98:101]
	v_mfma_f32_16x16x128_f8f6f4 v[146:149], v[2:9], v[172:179], v[146:149]
	v_mfma_f32_16x16x128_f8f6f4 v[150:153], v[10:17], v[172:179], v[150:153]
	v_mfma_f32_16x16x128_f8f6f4 v[142:145], v[10:17], v[190:197], v[142:145]
	v_mfma_f32_16x16x128_f8f6f4 v[138:141], v[2:9], v[190:197], v[138:141]
	v_mfma_f32_16x16x128_f8f6f4 v[130:133], v[2:9], v[198:205], v[130:133]
	v_mfma_f32_16x16x128_f8f6f4 v[134:137], v[10:17], v[198:205], v[134:137]
	s_setprio 0
	s_barrier
	s_add_i32 s72, s72, s43
	v_lshl_add_u64 v[172:173], s[8:9], 0, v[162:163]
	s_mov_b32 m0, s72
	ds_read_b128 v[190:193], v189 offset:16384
	ds_read_b128 v[194:197], v189 offset:17408
	ds_read_b128 v[198:201], v189 offset:18432
	ds_read_b128 v[202:205], v189 offset:19456
	ds_read_b128 v[206:209], v189 offset:20480
	ds_read_b128 v[210:213], v189 offset:21504
	ds_read_b128 v[214:217], v189 offset:22528
	ds_read_b128 v[218:221], v189 offset:23552
	global_load_lds_dwordx4 v[172:173], off
	s_add_i32 m0, s72, 0x2000
	s_add_u32 s74, s8, 0x158000
	v_lshl_add_u64 v[174:175], s[8:9], 0, v[166:167]
	s_addc_u32 s75, s9, 0
	s_add_i32 s72, s73, s43
	global_load_lds_dwordx4 v[174:175], off
	v_lshl_add_u64 v[176:177], s[74:75], 0, v[162:163]
	s_mov_b32 m0, s72
	v_lshl_add_u64 v[178:179], s[36:37], 0, v[166:167]
	global_load_lds_dwordx4 v[176:177], off
	v_lshl_add_u64 v[176:177], s[74:75], 0, v[166:167]
	s_add_i32 m0, s72, 0x2000
	s_nop 0
	global_load_lds_dwordx4 v[176:177], off
	v_lshl_add_u64 v[176:177], s[36:37], 0, v[162:163]
	s_mov_b32 m0, s64
	s_nop 0
	global_load_lds_dwordx4 v[176:177], off
	s_mov_b32 m0, s65
	s_nop 0
	global_load_lds_dwordx4 v[178:179], off
	s_waitcnt vmcnt(8)
	s_waitcnt lgkmcnt(0)
	s_barrier
	s_setprio 1
	s_waitcnt lgkmcnt(0)
	v_mfma_f32_16x16x128_f8f6f4 v[78:81], v[26:33], v[198:205], v[78:81]
	v_mfma_f32_16x16x128_f8f6f4 v[74:77], v[18:25], v[198:205], v[74:77]
	v_mfma_f32_16x16x128_f8f6f4 v[90:93], v[18:25], v[190:197], v[90:93]
	v_mfma_f32_16x16x128_f8f6f4 v[94:97], v[26:33], v[190:197], v[94:97]
	v_mfma_f32_16x16x128_f8f6f4 v[62:65], v[26:33], v[206:213], v[62:65]
	v_mfma_f32_16x16x128_f8f6f4 v[58:61], v[18:25], v[206:213], v[58:61]
	v_mfma_f32_16x16x128_f8f6f4 v[42:45], v[18:25], v[214:221], v[42:45]
	v_mfma_f32_16x16x128_f8f6f4 v[46:49], v[26:33], v[214:221], v[46:49]
	s_setprio 0
	s_setprio 1
	v_mfma_f32_16x16x128_f8f6f4 v[38:41], v[10:17], v[214:221], v[38:41]
	v_mfma_f32_16x16x128_f8f6f4 v[34:37], v[2:9], v[214:221], v[34:37]
	v_mfma_f32_16x16x128_f8f6f4 v[82:85], v[2:9], v[190:197], v[82:85]
	v_mfma_f32_16x16x128_f8f6f4 v[86:89], v[10:17], v[190:197], v[86:89]
	v_mfma_f32_16x16x128_f8f6f4 v[70:73], v[10:17], v[198:205], v[70:73]
	v_mfma_f32_16x16x128_f8f6f4 v[66:69], v[2:9], v[198:205], v[66:69]
	v_mfma_f32_16x16x128_f8f6f4 v[50:53], v[2:9], v[206:213], v[50:53]
	v_mfma_f32_16x16x128_f8f6f4 v[54:57], v[10:17], v[206:213], v[54:57]
	s_setprio 0
	s_barrier
	s_add_i32 s72, 0, 0x18000
	s_add_i32 s73, 0, 0x1c000
	v_add_u32_e32 v14, s72, v188
	v_add_u32_e32 v30, s73, v188
	ds_read_b128 v[2:5], v14
	ds_read_b128 v[6:9], v14 offset:1024
	ds_read_b128 v[10:13], v14 offset:2048
	ds_read_b128 v[14:17], v14 offset:3072
	ds_read_b128 v[18:21], v30
	ds_read_b128 v[22:25], v30 offset:1024
	ds_read_b128 v[26:29], v30 offset:2048
	ds_read_b128 v[30:33], v30 offset:3072
	s_add_u32 s36, s36, 0x158000
	s_addc_u32 s37, s37, 0
	s_mov_b32 m0, s66
	v_lshl_add_u64 v[222:223], s[36:37], 0, v[162:163]
	ds_read_b128 v[190:193], v189 offset:32768
	ds_read_b128 v[194:197], v189 offset:33792
	ds_read_b128 v[198:201], v189 offset:34816
	ds_read_b128 v[202:205], v189 offset:35840
	ds_read_b128 v[206:209], v189 offset:36864
	ds_read_b128 v[210:213], v189 offset:37888
	ds_read_b128 v[214:217], v189 offset:38912
	ds_read_b128 v[218:221], v189 offset:39936
	global_load_lds_dwordx4 v[222:223], off
	v_lshl_add_u64 v[222:223], s[36:37], 0, v[166:167]
	s_mov_b32 m0, s67
	s_nop 0
	global_load_lds_dwordx4 v[222:223], off
	s_waitcnt vmcnt(8)
	s_waitcnt lgkmcnt(0)
	s_barrier
	s_setprio 1
	s_waitcnt lgkmcnt(0)
	v_mfma_f32_16x16x128_f8f6f4 v[114:117], v[10:17], v[206:213], v[114:117]
	v_mfma_f32_16x16x128_f8f6f4 v[126:129], v[2:9], v[206:213], v[126:129]
	v_mfma_f32_16x16x128_f8f6f4 v[158:161], v[2:9], v[190:197], v[158:161]
	v_mfma_f32_16x16x128_f8f6f4 v[154:157], v[10:17], v[190:197], v[154:157]
	v_mfma_f32_16x16x128_f8f6f4 v[118:121], v[10:17], v[198:205], v[118:121]
	v_mfma_f32_16x16x128_f8f6f4 v[122:125], v[2:9], v[198:205], v[122:125]
	v_mfma_f32_16x16x128_f8f6f4 v[110:113], v[2:9], v[214:221], v[110:113]
	v_mfma_f32_16x16x128_f8f6f4 v[106:109], v[10:17], v[214:221], v[106:109]
	s_setprio 0
	s_setprio 1
	v_mfma_f32_16x16x128_f8f6f4 v[102:105], v[18:25], v[214:221], v[102:105]
	v_mfma_f32_16x16x128_f8f6f4 v[98:101], v[26:33], v[214:221], v[98:101]
	v_mfma_f32_16x16x128_f8f6f4 v[146:149], v[26:33], v[190:197], v[146:149]
	v_mfma_f32_16x16x128_f8f6f4 v[150:153], v[18:25], v[190:197], v[150:153]
	v_mfma_f32_16x16x128_f8f6f4 v[142:145], v[18:25], v[198:205], v[142:145]
	v_mfma_f32_16x16x128_f8f6f4 v[138:141], v[26:33], v[198:205], v[138:141]
	v_mfma_f32_16x16x128_f8f6f4 v[130:133], v[26:33], v[206:213], v[130:133]
	v_mfma_f32_16x16x128_f8f6f4 v[134:137], v[18:25], v[206:213], v[134:137]
	s_setprio 0
	s_barrier
	s_add_i32 s36, s72, s43
	v_lshl_add_u64 v[172:173], v[172:173], 0, s[22:23]
	s_mov_b32 m0, s36
	ds_read_b128 v[190:193], v189 offset:49152
	ds_read_b128 v[194:197], v189 offset:50176
	ds_read_b128 v[198:201], v189 offset:51200
	ds_read_b128 v[202:205], v189 offset:52224
	ds_read_b128 v[206:209], v189 offset:53248
	ds_read_b128 v[210:213], v189 offset:54272
	ds_read_b128 v[214:217], v189 offset:55296
	ds_read_b128 v[218:221], v189 offset:56320
	global_load_lds_dwordx4 v[172:173], off
	s_add_i32 m0, s36, 0x2000
	s_add_u32 s8, s8, 0x158080
	v_lshl_add_u64 v[172:173], v[174:175], 0, s[22:23]
	s_addc_u32 s9, s9, 0
	s_add_i32 s36, s73, s43
	global_load_lds_dwordx4 v[172:173], off
	v_lshl_add_u64 v[172:173], s[8:9], 0, v[162:163]
	s_mov_b32 m0, s36
	s_nop 0
	global_load_lds_dwordx4 v[172:173], off
	v_lshl_add_u64 v[172:173], s[8:9], 0, v[166:167]
	s_add_i32 m0, s36, 0x2000
	s_nop 0
	global_load_lds_dwordx4 v[172:173], off
	v_lshl_add_u64 v[172:173], v[176:177], 0, s[22:23]
	s_mov_b32 m0, s69
	s_nop 0
	global_load_lds_dwordx4 v[172:173], off
	v_lshl_add_u64 v[172:173], v[178:179], 0, s[22:23]
	s_mov_b32 m0, s70
	s_nop 0
	global_load_lds_dwordx4 v[172:173], off
	s_waitcnt vmcnt(8)
	s_waitcnt lgkmcnt(0)
	s_barrier
	s_setprio 1
	s_waitcnt lgkmcnt(0)
	v_mfma_f32_16x16x128_f8f6f4 v[62:65], v[2:9], v[206:213], v[62:65]
	v_mfma_f32_16x16x128_f8f6f4 v[58:61], v[10:17], v[206:213], v[58:61]
	v_mfma_f32_16x16x128_f8f6f4 v[90:93], v[10:17], v[190:197], v[90:93]
	v_mfma_f32_16x16x128_f8f6f4 v[94:97], v[2:9], v[190:197], v[94:97]
	v_mfma_f32_16x16x128_f8f6f4 v[78:81], v[2:9], v[198:205], v[78:81]
	v_mfma_f32_16x16x128_f8f6f4 v[74:77], v[10:17], v[198:205], v[74:77]
	v_mfma_f32_16x16x128_f8f6f4 v[42:45], v[10:17], v[214:221], v[42:45]
	v_mfma_f32_16x16x128_f8f6f4 v[46:49], v[2:9], v[214:221], v[46:49]
	s_setprio 0
	s_setprio 1
	v_mfma_f32_16x16x128_f8f6f4 v[38:41], v[18:25], v[214:221], v[38:41]
	v_mfma_f32_16x16x128_f8f6f4 v[34:37], v[26:33], v[214:221], v[34:37]
	v_mfma_f32_16x16x128_f8f6f4 v[82:85], v[26:33], v[190:197], v[82:85]
	v_mfma_f32_16x16x128_f8f6f4 v[86:89], v[18:25], v[190:197], v[86:89]
	v_mfma_f32_16x16x128_f8f6f4 v[70:73], v[18:25], v[198:205], v[70:73]
	v_mfma_f32_16x16x128_f8f6f4 v[66:69], v[26:33], v[198:205], v[66:69]
	v_mfma_f32_16x16x128_f8f6f4 v[50:53], v[26:33], v[206:213], v[50:53]
	v_mfma_f32_16x16x128_f8f6f4 v[54:57], v[18:25], v[206:213], v[54:57]
	s_setprio 0
	s_barrier
	s_add_i32 s71, s71, 2
	s_add_u32 s6, s6, 0x100
	s_addc_u32 s7, s7, 0
	s_cmpk_lt_u32 s71, 0x54
	s_cbranch_scc1 .LBB0_1745
	s_waitcnt vmcnt(0)
	s_cmpk_gt_u32 s40, 0xff
	s_cbranch_scc1 .LBB0_1748
	s_barrier
